# grid barrier leader: no wait between the (non-returning) TOPGEN add and the XGEN relay; on top of m16
# baseline (speedup 1.0000x reference)
; DI unsigned xb_ld(unsigned* p)              { return __hip_atomic_load(p, __ATOMIC_RELAXED, __HIP_MEMORY_SCOPE_AGENT); }
; DI unsigned xb_add(unsigned* p, unsigned v) { return __hip_atomic_fetch_add(p, v, __ATOMIC_RELAXED, __HIP_MEMORY_SCOPE_AGENT); }
; #define XB_SPIN(cond, bar) do { unsigned _sp = 0; while (cond) { __builtin_amdgcn_s_sleep(1); \
;     if ((++_sp & 255u) == 0u) { if (xb_ld(&(bar)[XB_TMO])) break; if (_sp > XB_SPIN_CAP) { atomicAdd(&(bar)[XB_TMO], 1u); break; } } } } while (0)
; DI void xcd_barrier(const XcdBarrier& b) {
;     ...
;             const unsigned og = xb_add(&bar[XB_TOP], 1u);
;             const unsigned tg = og / nx;
;             if (og + 1u == (tg + 1u) * nx) xb_add(&bar[XB_TOPGEN], 1u);
;             else XB_SPIN(xb_ld(&bar[XB_TOPGEN]) == tg, bar);
;             __builtin_amdgcn_fence(__ATOMIC_ACQUIRE, "agent");
;             xb_add(&bar[XB_XGEN(b.x)], 1u);
;             asm volatile("s_waitcnt vmcnt(0)" ::: "memory");
.LBB0_258:
	s_or_b64 exec, exec, s[30:31]
	v_readlane_b32 s4, v254, 12
	v_readlane_b32 s5, v254, 13
	v_mov_b32_e32 v1, 1
	s_nop 0
	v_mov_b64_e32 v[2:3], s[4:5]
	flat_atomic_add v[2:3], v1
	buffer_inv sc1
	s_waitcnt vmcnt(0)

; DI unsigned xb_ld(unsigned* p)              { return __hip_atomic_load(p, __ATOMIC_RELAXED, __HIP_MEMORY_SCOPE_AGENT); }
; DI unsigned xb_add(unsigned* p, unsigned v) { return __hip_atomic_fetch_add(p, v, __ATOMIC_RELAXED, __HIP_MEMORY_SCOPE_AGENT); }
; #define XB_SPIN(cond, bar) do { unsigned _sp = 0; while (cond) { __builtin_amdgcn_s_sleep(1); \
;     if ((++_sp & 255u) == 0u) { if (xb_ld(&(bar)[XB_TMO])) break; if (_sp > XB_SPIN_CAP) { atomicAdd(&(bar)[XB_TMO], 1u); break; } } } } while (0)
; DI void xcd_barrier(const XcdBarrier& b) {
;     ...
;             const unsigned og = xb_add(&bar[XB_TOP], 1u);
;             const unsigned tg = og / nx;
;             if (og + 1u == (tg + 1u) * nx) xb_add(&bar[XB_TOPGEN], 1u);
;             else XB_SPIN(xb_ld(&bar[XB_TOPGEN]) == tg, bar);
;             __builtin_amdgcn_fence(__ATOMIC_ACQUIRE, "agent");
;             xb_add(&bar[XB_XGEN(b.x)], 1u);
;             asm volatile("s_waitcnt vmcnt(0)" ::: "memory");
.LBB0_261:
	s_or_b64 exec, exec, s[16:17]
	v_readlane_b32 s4, v254, 12
	v_readlane_b32 s5, v254, 13
	v_mov_b32_e32 v1, 1
	s_nop 0
	v_mov_b64_e32 v[2:3], s[4:5]
	flat_atomic_add v[2:3], v1
	buffer_inv sc1
	s_waitcnt vmcnt(0)

; DI unsigned xb_ld(unsigned* p)              { return __hip_atomic_load(p, __ATOMIC_RELAXED, __HIP_MEMORY_SCOPE_AGENT); }
; DI unsigned xb_add(unsigned* p, unsigned v) { return __hip_atomic_fetch_add(p, v, __ATOMIC_RELAXED, __HIP_MEMORY_SCOPE_AGENT); }
; #define XB_SPIN(cond, bar) do { unsigned _sp = 0; while (cond) { __builtin_amdgcn_s_sleep(1); \
;     if ((++_sp & 255u) == 0u) { if (xb_ld(&(bar)[XB_TMO])) break; if (_sp > XB_SPIN_CAP) { atomicAdd(&(bar)[XB_TMO], 1u); break; } } } } while (0)
; DI void xcd_barrier(const XcdBarrier& b) {
;     ...
;             const unsigned og = xb_add(&bar[XB_TOP], 1u);
;             const unsigned tg = og / nx;
;             if (og + 1u == (tg + 1u) * nx) xb_add(&bar[XB_TOPGEN], 1u);
;             else XB_SPIN(xb_ld(&bar[XB_TOPGEN]) == tg, bar);
;             __builtin_amdgcn_fence(__ATOMIC_ACQUIRE, "agent");
;             xb_add(&bar[XB_XGEN(b.x)], 1u);
;             asm volatile("s_waitcnt vmcnt(0)" ::: "memory");
.LBB0_558:
	s_or_b64 exec, exec, s[30:31]
	v_readlane_b32 s6, v254, 12
	v_readlane_b32 s7, v254, 13
	v_mov_b32_e32 v1, 1
	s_nop 0
	v_mov_b64_e32 v[2:3], s[6:7]
	flat_atomic_add v[2:3], v1
	buffer_inv sc1
	s_waitcnt vmcnt(0)
